# baseline (speedup 1.0000x reference)
.LBB4_5:
.LBB4_12:
	s_cmpk_gt_u32 s3, 0xff
	s_cbranch_scc0 .Lrs_a_4
	s_barrier
.Lrs_a_4:
	s_add_u32 s81, s40, s22
	s_addc_u32 s82, s41, s23
	s_add_u32 s29, s40, 0x100
	s_addc_u32 s44, s41, 0
	s_and_b64 s[42:43], s[14:15], exec
	ds_read_b128 v[82:85], v161
	ds_read_b128 v[94:97], v161 offset:2048
	ds_read_b128 v[102:105], v162
	ds_read_b128 v[110:113], v162 offset:2048
	s_cselect_b32 s47, s37, s44
	s_cselect_b32 s46, s36, s29
	s_add_u32 s29, s38, 0x100
	s_addc_u32 s44, s39, 0
	s_and_b64 s[42:43], s[14:15], exec
	s_cselect_b32 s49, s5, s44
	s_cselect_b32 s48, s4, s29
	s_add_u32 s44, s46, 0x80
	s_addc_u32 s45, s47, 0
	s_add_u32 s42, s48, 0x80
	s_addc_u32 s43, s49, 0
	ds_read_b128 v[58:61], v163
	ds_read_b128 v[66:69], v163 offset:2048
	ds_read_b128 v[62:65], v164
	ds_read_b128 v[70:73], v164 offset:2048
	ds_read_b128 v[74:77], v163 offset:4096
	ds_read_b128 v[86:89], v163 offset:6144
	ds_read_b128 v[78:81], v164 offset:4096
	ds_read_b128 v[90:93], v164 offset:6144
	s_add_u32 s78, s81, 0x80
	s_addc_u32 s79, s82, 0
	s_mov_b32 m0, s70
	s_nop 0
	global_load_lds_dwordx4 v146, s[78:79]
	s_mov_b32 m0, s71
	s_nop 0
	global_load_lds_dwordx4 v150, s[78:79]
	s_waitcnt lgkmcnt(8)
	ds_read_b128 v[142:145], v161 offset:16384
	ds_read_b128 v[166:169], v161 offset:18432
	ds_read_b128 v[170:173], v162 offset:16384
	ds_read_b128 v[174:177], v162 offset:18432
	s_waitcnt vmcnt(8)
	s_waitcnt lgkmcnt(0)
	s_barrier
	s_waitcnt lgkmcnt(0)
	s_waitcnt vmcnt(16)
	v_mov_b32_e32 v1, v0
	v_pk_mul_f32 v[16:17], v[0:1], v[16:17]
	v_pk_mul_f32 v[14:15], v[154:155], v[14:15]
	v_pk_mul_f32 v[12:13], v[0:1], v[12:13]
	v_pk_mul_f32 v[10:11], v[154:155], v[10:11]
	v_pk_mul_f32 v[8:9], v[0:1], v[8:9]
	v_pk_mul_f32 v[6:7], v[154:155], v[6:7]
	v_pk_mul_f32 v[4:5], v[0:1], v[4:5]
	v_pk_mul_f32 v[2:3], v[154:155], v[2:3]
	v_mfma_f32_16x16x128_f8f6f4 v[18:21], v[82:85], v[58:61], v[14:17] cbsz:4 blgp:4
	v_mfma_f32_16x16x128_f8f6f4 v[18:21], v[102:105], v[62:65], v[18:21] cbsz:4 blgp:4
	v_mfma_f32_16x16x128_f8f6f4 v[22:25], v[94:97], v[58:61], v[10:13] cbsz:4 blgp:4
	v_mfma_f32_16x16x128_f8f6f4 v[22:25], v[110:113], v[62:65], v[22:25] cbsz:4 blgp:4
	v_mfma_f32_16x16x128_f8f6f4 v[26:29], v[82:85], v[66:69], v[14:17] cbsz:4 blgp:4
	v_mfma_f32_16x16x128_f8f6f4 v[26:29], v[102:105], v[70:73], v[26:29] cbsz:4 blgp:4
	v_mfma_f32_16x16x128_f8f6f4 v[30:33], v[94:97], v[66:69], v[10:13] cbsz:4 blgp:4
	v_mfma_f32_16x16x128_f8f6f4 v[30:33], v[110:113], v[70:73], v[30:33] cbsz:4 blgp:4
	v_mfma_f32_16x16x128_f8f6f4 v[34:37], v[82:85], v[74:77], v[14:17] cbsz:4 blgp:4
	v_mfma_f32_16x16x128_f8f6f4 v[34:37], v[102:105], v[78:81], v[34:37] cbsz:4 blgp:4
	v_mfma_f32_16x16x128_f8f6f4 v[38:41], v[94:97], v[74:77], v[10:13] cbsz:4 blgp:4
	v_mfma_f32_16x16x128_f8f6f4 v[38:41], v[110:113], v[78:81], v[38:41] cbsz:4 blgp:4
	v_mfma_f32_16x16x128_f8f6f4 v[42:45], v[82:85], v[86:89], v[14:17] cbsz:4 blgp:4
	v_mfma_f32_16x16x128_f8f6f4 v[42:45], v[102:105], v[90:93], v[42:45] cbsz:4 blgp:4
	v_mfma_f32_16x16x128_f8f6f4 v[46:49], v[94:97], v[86:89], v[10:13] cbsz:4 blgp:4
	v_mfma_f32_16x16x128_f8f6f4 v[46:49], v[110:113], v[90:93], v[46:49] cbsz:4 blgp:4
	v_mfma_f32_16x16x128_f8f6f4 v[50:53], v[142:145], v[58:61], v[6:9] cbsz:4 blgp:4
	v_mfma_f32_16x16x128_f8f6f4 v[50:53], v[170:173], v[62:65], v[50:53] cbsz:4 blgp:4
	v_mfma_f32_16x16x128_f8f6f4 v[54:57], v[166:169], v[58:61], v[2:5] cbsz:4 blgp:4
	v_mfma_f32_16x16x128_f8f6f4 v[54:57], v[174:177], v[62:65], v[54:57] cbsz:4 blgp:4
	v_mfma_f32_16x16x128_f8f6f4 v[58:61], v[142:145], v[66:69], v[6:9] cbsz:4 blgp:4
	v_mfma_f32_16x16x128_f8f6f4 v[58:61], v[170:173], v[70:73], v[58:61] cbsz:4 blgp:4
	v_mfma_f32_16x16x128_f8f6f4 v[62:65], v[166:169], v[66:69], v[2:5] cbsz:4 blgp:4
	v_mfma_f32_16x16x128_f8f6f4 v[62:65], v[174:177], v[70:73], v[62:65] cbsz:4 blgp:4
	v_mfma_f32_16x16x128_f8f6f4 v[66:69], v[142:145], v[74:77], v[6:9] cbsz:4 blgp:4
	v_mfma_f32_16x16x128_f8f6f4 v[66:69], v[170:173], v[78:81], v[66:69] cbsz:4 blgp:4
	v_mfma_f32_16x16x128_f8f6f4 v[70:73], v[166:169], v[74:77], v[2:5] cbsz:4 blgp:4
	v_mfma_f32_16x16x128_f8f6f4 v[70:73], v[174:177], v[78:81], v[70:73] cbsz:4 blgp:4
	v_mfma_f32_16x16x128_f8f6f4 v[74:77], v[142:145], v[86:89], v[6:9] cbsz:4 blgp:4
	v_mfma_f32_16x16x128_f8f6f4 v[74:77], v[170:173], v[90:93], v[74:77] cbsz:4 blgp:4
	v_mfma_f32_16x16x128_f8f6f4 v[78:81], v[166:169], v[86:89], v[2:5] cbsz:4 blgp:4
	v_mfma_f32_16x16x128_f8f6f4 v[78:81], v[174:177], v[90:93], v[78:81] cbsz:4 blgp:4
	s_barrier
	s_mov_b32 m0, s55
	s_nop 0
	global_load_lds_dwordx4 v148, s[48:49]
	s_mov_b32 m0, s56
	s_nop 0
	global_load_lds_dwordx4 v152, s[48:49]
	ds_read_b128 v[114:117], v163 offset:16384
	ds_read_b128 v[122:125], v163 offset:18432
	ds_read_b128 v[130:133], v164 offset:16384
	ds_read_b128 v[134:137], v164 offset:18432
	ds_read_b128 v[178:181], v163 offset:20480
	ds_read_b128 v[182:185], v163 offset:22528
	ds_read_b128 v[186:189], v164 offset:20480
	ds_read_b128 v[190:193], v164 offset:22528
	s_mov_b32 m0, s54
	s_nop 0
	global_load_lds_dwordx4 v146, s[46:47]
	s_mov_b32 m0, s57
	s_nop 0
	global_load_lds_dwordx4 v150, s[46:47]
	s_add_u32 s48, s48, s24
	s_addc_u32 s49, s49, s25
	s_mov_b32 m0, s58
	s_nop 0
	global_load_lds_dwordx4 v148, s[48:49]
	s_mov_b32 m0, s59
	s_nop 0
	global_load_lds_dwordx4 v152, s[48:49]
	s_waitcnt vmcnt(8)
	s_waitcnt lgkmcnt(0)
	s_barrier
	v_mfma_f32_16x16x128_f8f6f4 v[86:89], v[82:85], v[114:117], v[14:17] cbsz:4 blgp:4
	v_mfma_f32_16x16x128_f8f6f4 v[86:89], v[102:105], v[130:133], v[86:89] cbsz:4 blgp:4
	v_mfma_f32_16x16x128_f8f6f4 v[90:93], v[94:97], v[114:117], v[10:13] cbsz:4 blgp:4
	v_mfma_f32_16x16x128_f8f6f4 v[90:93], v[110:113], v[130:133], v[90:93] cbsz:4 blgp:4
	v_mfma_f32_16x16x128_f8f6f4 v[98:101], v[82:85], v[122:125], v[14:17] cbsz:4 blgp:4
	v_mfma_f32_16x16x128_f8f6f4 v[98:101], v[102:105], v[134:137], v[98:101] cbsz:4 blgp:4
	v_mfma_f32_16x16x128_f8f6f4 v[106:109], v[94:97], v[122:125], v[10:13] cbsz:4 blgp:4
	v_mfma_f32_16x16x128_f8f6f4 v[106:109], v[110:113], v[134:137], v[106:109] cbsz:4 blgp:4
	v_mfma_f32_16x16x128_f8f6f4 v[118:121], v[82:85], v[178:181], v[14:17] cbsz:4 blgp:4
	v_mfma_f32_16x16x128_f8f6f4 v[118:121], v[102:105], v[186:189], v[118:121] cbsz:4 blgp:4
	v_mfma_f32_16x16x128_f8f6f4 v[126:129], v[94:97], v[178:181], v[10:13] cbsz:4 blgp:4
	v_mfma_f32_16x16x128_f8f6f4 v[126:129], v[110:113], v[186:189], v[126:129] cbsz:4 blgp:4
	v_mfma_f32_16x16x128_f8f6f4 v[138:141], v[82:85], v[182:185], v[14:17] cbsz:4 blgp:4
	v_mfma_f32_16x16x128_f8f6f4 v[138:141], v[102:105], v[190:193], v[138:141] cbsz:4 blgp:4
	v_mfma_f32_16x16x128_f8f6f4 v[82:85], v[94:97], v[182:185], v[10:13] cbsz:4 blgp:4
	v_mfma_f32_16x16x128_f8f6f4 v[82:85], v[110:113], v[190:193], v[82:85] cbsz:4 blgp:4
	v_mfma_f32_16x16x128_f8f6f4 v[94:97], v[142:145], v[114:117], v[6:9] cbsz:4 blgp:4
	v_mfma_f32_16x16x128_f8f6f4 v[94:97], v[170:173], v[130:133], v[94:97] cbsz:4 blgp:4
	v_mfma_f32_16x16x128_f8f6f4 v[102:105], v[166:169], v[114:117], v[2:5] cbsz:4 blgp:4
	v_mfma_f32_16x16x128_f8f6f4 v[102:105], v[174:177], v[130:133], v[102:105] cbsz:4 blgp:4
	v_mfma_f32_16x16x128_f8f6f4 v[110:113], v[142:145], v[122:125], v[6:9] cbsz:4 blgp:4
	v_mfma_f32_16x16x128_f8f6f4 v[110:113], v[170:173], v[134:137], v[110:113] cbsz:4 blgp:4
	v_mfma_f32_16x16x128_f8f6f4 v[114:117], v[166:169], v[122:125], v[2:5] cbsz:4 blgp:4
	v_mfma_f32_16x16x128_f8f6f4 v[114:117], v[174:177], v[134:137], v[114:117] cbsz:4 blgp:4
	v_mfma_f32_16x16x128_f8f6f4 v[122:125], v[142:145], v[178:181], v[6:9] cbsz:4 blgp:4
	v_mfma_f32_16x16x128_f8f6f4 v[122:125], v[170:173], v[186:189], v[122:125] cbsz:4 blgp:4
	v_mfma_f32_16x16x128_f8f6f4 v[130:133], v[166:169], v[178:181], v[2:5] cbsz:4 blgp:4
	v_mfma_f32_16x16x128_f8f6f4 v[130:133], v[174:177], v[186:189], v[130:133] cbsz:4 blgp:4
	v_mfma_f32_16x16x128_f8f6f4 v[134:137], v[142:145], v[182:185], v[6:9] cbsz:4 blgp:4
	v_mfma_f32_16x16x128_f8f6f4 v[134:137], v[170:173], v[190:193], v[134:137] cbsz:4 blgp:4
	v_mfma_f32_16x16x128_f8f6f4 v[142:145], v[166:169], v[182:185], v[2:5] cbsz:4 blgp:4
	v_mfma_f32_16x16x128_f8f6f4 v[142:145], v[174:177], v[190:193], v[142:145] cbsz:4 blgp:4
	s_barrier
	s_add_i32 s53, s53, 1
	s_mul_i32 s0, s53, s72
	s_mul_hi_u32 s1, s53, s33
	s_add_i32 s1, s1, s0
	s_mul_i32 s0, s53, s33
	s_add_u32 s4, s0, s2
	s_addc_u32 s5, s1, s73
	v_mov_b64_e32 v[230:231], s[20:21]
	v_cmp_ge_i64_e32 vcc, s[4:5], v[230:231]
	s_and_b64 s[0:1], exec, vcc
	s_mov_b64 vcc, s[0:1]
	s_cbranch_vccnz .LBB4_7
	s_and_b32 s13, s4, 7
	s_lshl_b32 s13, s13, s50
	s_ashr_i32 s28, s4, 3
	s_add_i32 s13, s13, s28
	s_ashr_i32 s28, s13, s51
	s_and_b32 s13, s13, s62
	s_lshl_b32 s28, s28, 3
	s_and_b32 s29, s13, 7
	s_or_b32 s74, s28, s29
	s_ashr_i32 s28, s74, s52
	s_lshr_b32 s13, s13, 3
	s_mul_i32 s28, s28, s6
	s_and_b32 s75, s74, s7
	s_add_i32 s28, s28, s13
.LBB4_7:
	v_mov_b64_e32 v[230:231], s[20:21]
	v_cmp_lt_i64_e32 vcc, s[4:5], v[230:231]
	s_mov_b64 s[36:37], s[40:41]
	s_nop 0
	v_cndmask_b32_e64 v230, 0, 1, vcc
	v_cmp_ne_u32_e64 s[4:5], 1, v230
	s_andn2_b64 vcc, exec, vcc
	s_cbranch_vccz .LBB4_10
	s_and_b64 vcc, exec, s[4:5]
	s_mov_b64 s[4:5], s[38:39]
	s_cbranch_vccz .LBB4_11
.LBB4_9:
	s_branch .Lsd_4

.Lsd_4:
	ds_read_b128 v[166:169], v161 offset:32768
	ds_read_b128 v[170:173], v161 offset:34816
	ds_read_b128 v[174:177], v162 offset:32768
	ds_read_b128 v[178:181], v162 offset:34816
	ds_read_b128 v[182:185], v163 offset:32768
	ds_read_b128 v[186:189], v163 offset:34816
	ds_read_b128 v[190:193], v164 offset:32768
	ds_read_b128 v[194:197], v164 offset:34816
	ds_read_b128 v[198:201], v163 offset:36864
	ds_read_b128 v[202:205], v163 offset:38912
	ds_read_b128 v[206:209], v164 offset:36864
	ds_read_b128 v[210:213], v164 offset:38912
	s_add_u32 s46, s46, s22
	s_addc_u32 s47, s47, s23
	s_mov_b32 m0, s60
	s_nop 0
	global_load_lds_dwordx4 v146, s[46:47]
	s_mov_b32 m0, s61
	s_nop 0
	global_load_lds_dwordx4 v150, s[46:47]
	s_waitcnt lgkmcnt(8)
	ds_read_b128 v[214:217], v161 offset:49152
	ds_read_b128 v[218:221], v161 offset:51200
	ds_read_b128 v[222:225], v162 offset:49152
	ds_read_b128 v[226:229], v162 offset:51200
	s_waitcnt vmcnt(8)
	s_waitcnt lgkmcnt(0)
	s_barrier
	s_waitcnt lgkmcnt(0)
	v_mfma_f32_16x16x128_f8f6f4 v[18:21], v[166:169], v[182:185], v[18:21] cbsz:4 blgp:4
	v_mfma_f32_16x16x128_f8f6f4 v[18:21], v[174:177], v[190:193], v[18:21] cbsz:4 blgp:4
	v_mfma_f32_16x16x128_f8f6f4 v[22:25], v[170:173], v[182:185], v[22:25] cbsz:4 blgp:4
	v_mfma_f32_16x16x128_f8f6f4 v[22:25], v[178:181], v[190:193], v[22:25] cbsz:4 blgp:4
	v_mfma_f32_16x16x128_f8f6f4 v[26:29], v[166:169], v[186:189], v[26:29] cbsz:4 blgp:4
	v_mfma_f32_16x16x128_f8f6f4 v[26:29], v[174:177], v[194:197], v[26:29] cbsz:4 blgp:4
	v_mfma_f32_16x16x128_f8f6f4 v[30:33], v[170:173], v[186:189], v[30:33] cbsz:4 blgp:4
	v_mfma_f32_16x16x128_f8f6f4 v[30:33], v[178:181], v[194:197], v[30:33] cbsz:4 blgp:4
	v_mfma_f32_16x16x128_f8f6f4 v[34:37], v[166:169], v[198:201], v[34:37] cbsz:4 blgp:4
	v_mfma_f32_16x16x128_f8f6f4 v[34:37], v[174:177], v[206:209], v[34:37] cbsz:4 blgp:4
	v_mfma_f32_16x16x128_f8f6f4 v[38:41], v[170:173], v[198:201], v[38:41] cbsz:4 blgp:4
	v_mfma_f32_16x16x128_f8f6f4 v[38:41], v[178:181], v[206:209], v[38:41] cbsz:4 blgp:4
	v_mfma_f32_16x16x128_f8f6f4 v[42:45], v[166:169], v[202:205], v[42:45] cbsz:4 blgp:4
	v_mfma_f32_16x16x128_f8f6f4 v[42:45], v[174:177], v[210:213], v[42:45] cbsz:4 blgp:4
	v_mfma_f32_16x16x128_f8f6f4 v[46:49], v[170:173], v[202:205], v[46:49] cbsz:4 blgp:4
	v_mfma_f32_16x16x128_f8f6f4 v[46:49], v[178:181], v[210:213], v[46:49] cbsz:4 blgp:4
	v_mfma_f32_16x16x128_f8f6f4 v[50:53], v[214:217], v[182:185], v[50:53] cbsz:4 blgp:4
	v_mfma_f32_16x16x128_f8f6f4 v[50:53], v[222:225], v[190:193], v[50:53] cbsz:4 blgp:4
	v_mfma_f32_16x16x128_f8f6f4 v[54:57], v[218:221], v[182:185], v[54:57] cbsz:4 blgp:4
	v_mfma_f32_16x16x128_f8f6f4 v[54:57], v[226:229], v[190:193], v[54:57] cbsz:4 blgp:4
	v_mfma_f32_16x16x128_f8f6f4 v[58:61], v[214:217], v[186:189], v[58:61] cbsz:4 blgp:4
	v_mfma_f32_16x16x128_f8f6f4 v[58:61], v[222:225], v[194:197], v[58:61] cbsz:4 blgp:4
	v_mfma_f32_16x16x128_f8f6f4 v[62:65], v[218:221], v[186:189], v[62:65] cbsz:4 blgp:4
	v_mfma_f32_16x16x128_f8f6f4 v[62:65], v[226:229], v[194:197], v[62:65] cbsz:4 blgp:4
	v_mfma_f32_16x16x128_f8f6f4 v[66:69], v[214:217], v[198:201], v[66:69] cbsz:4 blgp:4
	v_mfma_f32_16x16x128_f8f6f4 v[66:69], v[222:225], v[206:209], v[66:69] cbsz:4 blgp:4
	v_mfma_f32_16x16x128_f8f6f4 v[70:73], v[218:221], v[198:201], v[70:73] cbsz:4 blgp:4
	v_mfma_f32_16x16x128_f8f6f4 v[70:73], v[226:229], v[206:209], v[70:73] cbsz:4 blgp:4
	v_mfma_f32_16x16x128_f8f6f4 v[74:77], v[214:217], v[202:205], v[74:77] cbsz:4 blgp:4
	v_mfma_f32_16x16x128_f8f6f4 v[74:77], v[222:225], v[210:213], v[74:77] cbsz:4 blgp:4
	v_mfma_f32_16x16x128_f8f6f4 v[78:81], v[218:221], v[202:205], v[78:81] cbsz:4 blgp:4
	v_mfma_f32_16x16x128_f8f6f4 v[78:81], v[226:229], v[210:213], v[78:81] cbsz:4 blgp:4
	s_barrier
	s_mov_b32 m0, s64
	s_nop 0
	global_load_lds_dwordx4 v148, s[42:43]
	s_mov_b32 m0, s65
	s_nop 0
	global_load_lds_dwordx4 v152, s[42:43]
	ds_read_b128 v[182:185], v163 offset:49152
	ds_read_b128 v[186:189], v163 offset:51200
	ds_read_b128 v[190:193], v164 offset:49152
	ds_read_b128 v[194:197], v164 offset:51200
	ds_read_b128 v[198:201], v163 offset:53248
	ds_read_b128 v[202:205], v163 offset:55296
	ds_read_b128 v[206:209], v164 offset:53248
	ds_read_b128 v[210:213], v164 offset:55296
	s_mov_b32 m0, s66
	s_nop 0
	global_load_lds_dwordx4 v146, s[44:45]
	s_mov_b32 m0, s67
	s_nop 0
	global_load_lds_dwordx4 v150, s[44:45]
	s_add_u32 s42, s42, s24
	s_addc_u32 s43, s43, s25
	s_mov_b32 m0, s68
	s_nop 0
	global_load_lds_dwordx4 v148, s[42:43]
	s_mov_b32 m0, s69
	s_nop 0
	global_load_lds_dwordx4 v152, s[42:43]
	s_waitcnt vmcnt(8)
	s_waitcnt lgkmcnt(0)
	s_barrier
	v_mfma_f32_16x16x128_f8f6f4 v[86:89], v[166:169], v[182:185], v[86:89] cbsz:4 blgp:4
	v_mfma_f32_16x16x128_f8f6f4 v[86:89], v[174:177], v[190:193], v[86:89] cbsz:4 blgp:4
	v_mfma_f32_16x16x128_f8f6f4 v[90:93], v[170:173], v[182:185], v[90:93] cbsz:4 blgp:4
	v_mfma_f32_16x16x128_f8f6f4 v[90:93], v[178:181], v[190:193], v[90:93] cbsz:4 blgp:4
	v_mfma_f32_16x16x128_f8f6f4 v[98:101], v[166:169], v[186:189], v[98:101] cbsz:4 blgp:4
	v_mfma_f32_16x16x128_f8f6f4 v[98:101], v[174:177], v[194:197], v[98:101] cbsz:4 blgp:4
	v_mfma_f32_16x16x128_f8f6f4 v[106:109], v[170:173], v[186:189], v[106:109] cbsz:4 blgp:4
	v_mfma_f32_16x16x128_f8f6f4 v[106:109], v[178:181], v[194:197], v[106:109] cbsz:4 blgp:4
	v_mfma_f32_16x16x128_f8f6f4 v[118:121], v[166:169], v[198:201], v[118:121] cbsz:4 blgp:4
	v_mfma_f32_16x16x128_f8f6f4 v[118:121], v[174:177], v[206:209], v[118:121] cbsz:4 blgp:4
	v_mfma_f32_16x16x128_f8f6f4 v[126:129], v[170:173], v[198:201], v[126:129] cbsz:4 blgp:4
	v_mfma_f32_16x16x128_f8f6f4 v[126:129], v[178:181], v[206:209], v[126:129] cbsz:4 blgp:4
	v_mfma_f32_16x16x128_f8f6f4 v[138:141], v[166:169], v[202:205], v[138:141] cbsz:4 blgp:4
	v_mfma_f32_16x16x128_f8f6f4 v[138:141], v[174:177], v[210:213], v[138:141] cbsz:4 blgp:4
	v_mfma_f32_16x16x128_f8f6f4 v[82:85], v[170:173], v[202:205], v[82:85] cbsz:4 blgp:4
	v_mfma_f32_16x16x128_f8f6f4 v[82:85], v[178:181], v[210:213], v[82:85] cbsz:4 blgp:4
	v_mfma_f32_16x16x128_f8f6f4 v[94:97], v[214:217], v[182:185], v[94:97] cbsz:4 blgp:4
	v_mfma_f32_16x16x128_f8f6f4 v[94:97], v[222:225], v[190:193], v[94:97] cbsz:4 blgp:4
	v_mfma_f32_16x16x128_f8f6f4 v[102:105], v[218:221], v[182:185], v[102:105] cbsz:4 blgp:4
	v_mfma_f32_16x16x128_f8f6f4 v[102:105], v[226:229], v[190:193], v[102:105] cbsz:4 blgp:4
	v_mfma_f32_16x16x128_f8f6f4 v[110:113], v[214:217], v[186:189], v[110:113] cbsz:4 blgp:4
	v_mfma_f32_16x16x128_f8f6f4 v[110:113], v[222:225], v[194:197], v[110:113] cbsz:4 blgp:4
	v_mfma_f32_16x16x128_f8f6f4 v[114:117], v[218:221], v[186:189], v[114:117] cbsz:4 blgp:4
	v_mfma_f32_16x16x128_f8f6f4 v[114:117], v[226:229], v[194:197], v[114:117] cbsz:4 blgp:4
	v_mfma_f32_16x16x128_f8f6f4 v[122:125], v[214:217], v[198:201], v[122:125] cbsz:4 blgp:4
	v_mfma_f32_16x16x128_f8f6f4 v[122:125], v[222:225], v[206:209], v[122:125] cbsz:4 blgp:4
	v_mfma_f32_16x16x128_f8f6f4 v[130:133], v[218:221], v[198:201], v[130:133] cbsz:4 blgp:4
	v_mfma_f32_16x16x128_f8f6f4 v[130:133], v[226:229], v[206:209], v[130:133] cbsz:4 blgp:4
	v_mfma_f32_16x16x128_f8f6f4 v[134:137], v[214:217], v[202:205], v[134:137] cbsz:4 blgp:4
	v_mfma_f32_16x16x128_f8f6f4 v[134:137], v[222:225], v[210:213], v[134:137] cbsz:4 blgp:4
	v_mfma_f32_16x16x128_f8f6f4 v[142:145], v[218:221], v[202:205], v[142:145] cbsz:4 blgp:4
	v_mfma_f32_16x16x128_f8f6f4 v[142:145], v[226:229], v[210:213], v[142:145] cbsz:4 blgp:4
	s_andn2_b64 vcc, exec, s[34:35]
	s_barrier
	s_cbranch_vccnz .LBB4_4
	s_ashr_i32 s29, s28, 31
	s_lshl_b64 s[42:43], s[28:29], 10
	s_add_u32 s42, s10, s42
	s_addc_u32 s43, s11, s43
	s_add_u32 s29, s40, 0x200
	s_addc_u32 s78, s41, 0
	s_add_u32 s79, s38, 0x200
	s_addc_u32 s80, s39, 0
	s_add_u32 s38, s81, 0x180
	s_addc_u32 s39, s82, 0
	s_mov_b32 s81, 4
	s_cmp_eq_u32 s63, s81
	s_cselect_b64 s[40:41], -1, 0
	s_cmp_lg_u32 s63, s81
	s_cbranch_scc1 .LBB4_15

	.amdhsa_kernel _Z6k_gemmI4Epi8ILi0ELb1ELb1EEEv4GemmT_iiii
		.amdhsa_group_segment_fixed_size 0
		.amdhsa_private_segment_fixed_size 0
		.amdhsa_kernarg_size 328
		.amdhsa_user_sgpr_count 2
		.amdhsa_user_sgpr_dispatch_ptr 0
		.amdhsa_user_sgpr_queue_ptr 0
		.amdhsa_user_sgpr_kernarg_segment_ptr 1
		.amdhsa_user_sgpr_dispatch_id 0
		.amdhsa_user_sgpr_kernarg_preload_length 0
		.amdhsa_user_sgpr_kernarg_preload_offset 0
		.amdhsa_user_sgpr_private_segment_size 0
		.amdhsa_uses_dynamic_stack 0
		.amdhsa_enable_private_segment 0
		.amdhsa_system_sgpr_workgroup_id_x 1
		.amdhsa_system_sgpr_workgroup_id_y 0
		.amdhsa_system_sgpr_workgroup_id_z 0
		.amdhsa_system_sgpr_workgroup_info 0
		.amdhsa_system_vgpr_workitem_id 0
		.amdhsa_next_free_vgpr 232
		.amdhsa_next_free_sgpr 83
		.amdhsa_accum_offset 232
		.amdhsa_reserve_vcc 1
		.amdhsa_float_round_mode_32 0
		.amdhsa_float_round_mode_16_64 0
		.amdhsa_float_denorm_mode_32 3
		.amdhsa_float_denorm_mode_16_64 3
		.amdhsa_dx10_clamp 1
		.amdhsa_ieee_mode 1
		.amdhsa_fp16_overflow 0
		.amdhsa_tg_split 0
		.amdhsa_exception_fp_ieee_invalid_op 0
		.amdhsa_exception_fp_denorm_src 0
		.amdhsa_exception_fp_ieee_div_zero 0
		.amdhsa_exception_fp_ieee_overflow 0
		.amdhsa_exception_fp_ieee_underflow 0
		.amdhsa_exception_fp_ieee_inexact 0
		.amdhsa_exception_int_div_zero 0
	.end_amdhsa_kernel

.Lrs_a_5:
	s_add_u32 s82, s42, s22
	s_addc_u32 s83, s43, s23
	s_add_u32 s29, s42, 0x100
	s_addc_u32 s46, s43, 0
	s_and_b64 s[44:45], s[14:15], exec
	ds_read_b128 v[82:85], v163
	ds_read_b128 v[94:97], v163 offset:2048
	ds_read_b128 v[102:105], v164
	ds_read_b128 v[110:113], v164 offset:2048
	s_cselect_b32 s49, s39, s46
	s_cselect_b32 s48, s38, s29
	s_add_u32 s29, s40, 0x100
	s_addc_u32 s46, s41, 0
	s_and_b64 s[44:45], s[14:15], exec
	s_cselect_b32 s51, s5, s46
	s_cselect_b32 s50, s4, s29
	s_add_u32 s46, s48, 0x80
	s_addc_u32 s47, s49, 0
	s_add_u32 s44, s50, 0x80
	s_addc_u32 s45, s51, 0
	ds_read_b128 v[58:61], v165
	ds_read_b128 v[66:69], v165 offset:2048
	ds_read_b128 v[62:65], v166
	ds_read_b128 v[70:73], v166 offset:2048
	ds_read_b128 v[74:77], v165 offset:4096
	ds_read_b128 v[86:89], v165 offset:6144
	ds_read_b128 v[78:81], v166 offset:4096
	ds_read_b128 v[90:93], v166 offset:6144
	s_add_u32 s80, s82, 0x80
	s_addc_u32 s81, s83, 0
	s_mov_b32 m0, s71
	s_nop 0
	global_load_lds_dwordx4 v146, s[80:81]
	s_mov_b32 m0, s72
	s_nop 0
	global_load_lds_dwordx4 v150, s[80:81]
	s_waitcnt lgkmcnt(8)
	ds_read_b128 v[142:145], v163 offset:16384
	ds_read_b128 v[156:159], v163 offset:18432
	ds_read_b128 v[168:171], v164 offset:16384
	ds_read_b128 v[172:175], v164 offset:18432
	s_waitcnt vmcnt(8)
	s_waitcnt lgkmcnt(0)
	s_barrier
	s_waitcnt lgkmcnt(0)
	s_waitcnt vmcnt(16)
	v_mov_b32_e32 v1, v0
	v_pk_mul_f32 v[16:17], v[0:1], v[16:17]
	v_pk_mul_f32 v[14:15], v[154:155], v[14:15]
	v_pk_mul_f32 v[12:13], v[0:1], v[12:13]
	v_pk_mul_f32 v[10:11], v[154:155], v[10:11]
	v_pk_mul_f32 v[8:9], v[0:1], v[8:9]
	v_pk_mul_f32 v[6:7], v[154:155], v[6:7]
	v_pk_mul_f32 v[4:5], v[0:1], v[4:5]
	v_pk_mul_f32 v[2:3], v[154:155], v[2:3]
	v_mfma_f32_16x16x128_f8f6f4 v[18:21], v[82:85], v[58:61], v[14:17] cbsz:4 blgp:4
	v_mfma_f32_16x16x128_f8f6f4 v[18:21], v[102:105], v[62:65], v[18:21] cbsz:4 blgp:4
	v_mfma_f32_16x16x128_f8f6f4 v[22:25], v[94:97], v[58:61], v[10:13] cbsz:4 blgp:4
	v_mfma_f32_16x16x128_f8f6f4 v[22:25], v[110:113], v[62:65], v[22:25] cbsz:4 blgp:4
	v_mfma_f32_16x16x128_f8f6f4 v[26:29], v[82:85], v[66:69], v[14:17] cbsz:4 blgp:4
	v_mfma_f32_16x16x128_f8f6f4 v[26:29], v[102:105], v[70:73], v[26:29] cbsz:4 blgp:4
	v_mfma_f32_16x16x128_f8f6f4 v[30:33], v[94:97], v[66:69], v[10:13] cbsz:4 blgp:4
	v_mfma_f32_16x16x128_f8f6f4 v[30:33], v[110:113], v[70:73], v[30:33] cbsz:4 blgp:4
	v_mfma_f32_16x16x128_f8f6f4 v[34:37], v[82:85], v[74:77], v[14:17] cbsz:4 blgp:4
	v_mfma_f32_16x16x128_f8f6f4 v[34:37], v[102:105], v[78:81], v[34:37] cbsz:4 blgp:4
	v_mfma_f32_16x16x128_f8f6f4 v[38:41], v[94:97], v[74:77], v[10:13] cbsz:4 blgp:4
	v_mfma_f32_16x16x128_f8f6f4 v[38:41], v[110:113], v[78:81], v[38:41] cbsz:4 blgp:4
	v_mfma_f32_16x16x128_f8f6f4 v[42:45], v[82:85], v[86:89], v[14:17] cbsz:4 blgp:4
	v_mfma_f32_16x16x128_f8f6f4 v[42:45], v[102:105], v[90:93], v[42:45] cbsz:4 blgp:4
	v_mfma_f32_16x16x128_f8f6f4 v[46:49], v[94:97], v[86:89], v[10:13] cbsz:4 blgp:4
	v_mfma_f32_16x16x128_f8f6f4 v[46:49], v[110:113], v[90:93], v[46:49] cbsz:4 blgp:4
	v_mfma_f32_16x16x128_f8f6f4 v[50:53], v[142:145], v[58:61], v[6:9] cbsz:4 blgp:4
	v_mfma_f32_16x16x128_f8f6f4 v[50:53], v[168:171], v[62:65], v[50:53] cbsz:4 blgp:4
	v_mfma_f32_16x16x128_f8f6f4 v[54:57], v[156:159], v[58:61], v[2:5] cbsz:4 blgp:4
	v_mfma_f32_16x16x128_f8f6f4 v[54:57], v[172:175], v[62:65], v[54:57] cbsz:4 blgp:4
	v_mfma_f32_16x16x128_f8f6f4 v[58:61], v[142:145], v[66:69], v[6:9] cbsz:4 blgp:4
	v_mfma_f32_16x16x128_f8f6f4 v[58:61], v[168:171], v[70:73], v[58:61] cbsz:4 blgp:4
	v_mfma_f32_16x16x128_f8f6f4 v[62:65], v[156:159], v[66:69], v[2:5] cbsz:4 blgp:4
	v_mfma_f32_16x16x128_f8f6f4 v[62:65], v[172:175], v[70:73], v[62:65] cbsz:4 blgp:4
	v_mfma_f32_16x16x128_f8f6f4 v[66:69], v[142:145], v[74:77], v[6:9] cbsz:4 blgp:4
	v_mfma_f32_16x16x128_f8f6f4 v[66:69], v[168:171], v[78:81], v[66:69] cbsz:4 blgp:4
	v_mfma_f32_16x16x128_f8f6f4 v[70:73], v[156:159], v[74:77], v[2:5] cbsz:4 blgp:4
	v_mfma_f32_16x16x128_f8f6f4 v[70:73], v[172:175], v[78:81], v[70:73] cbsz:4 blgp:4
	v_mfma_f32_16x16x128_f8f6f4 v[74:77], v[142:145], v[86:89], v[6:9] cbsz:4 blgp:4
	v_mfma_f32_16x16x128_f8f6f4 v[74:77], v[168:171], v[90:93], v[74:77] cbsz:4 blgp:4
	v_mfma_f32_16x16x128_f8f6f4 v[78:81], v[156:159], v[86:89], v[2:5] cbsz:4 blgp:4
	v_mfma_f32_16x16x128_f8f6f4 v[78:81], v[172:175], v[90:93], v[78:81] cbsz:4 blgp:4
	s_barrier
	s_mov_b32 m0, s56
	s_nop 0
	global_load_lds_dwordx4 v148, s[50:51]
	s_mov_b32 m0, s57
	s_nop 0
	global_load_lds_dwordx4 v152, s[50:51]
	ds_read_b128 v[114:117], v165 offset:16384
	ds_read_b128 v[122:125], v165 offset:18432
	ds_read_b128 v[130:133], v166 offset:16384
	ds_read_b128 v[134:137], v166 offset:18432
	ds_read_b128 v[176:179], v165 offset:20480
	ds_read_b128 v[180:183], v165 offset:22528
	ds_read_b128 v[184:187], v166 offset:20480
	ds_read_b128 v[188:191], v166 offset:22528
	s_mov_b32 m0, s55
	s_nop 0
	global_load_lds_dwordx4 v146, s[48:49]
	s_mov_b32 m0, s58
	s_nop 0
	global_load_lds_dwordx4 v150, s[48:49]
	s_add_u32 s50, s50, s24
	s_addc_u32 s51, s51, s25
	s_mov_b32 m0, s59
	s_nop 0
	global_load_lds_dwordx4 v148, s[50:51]
	s_mov_b32 m0, s60
	s_nop 0
	global_load_lds_dwordx4 v152, s[50:51]
	s_waitcnt vmcnt(8)
	s_waitcnt lgkmcnt(0)
	s_barrier
	v_mfma_f32_16x16x128_f8f6f4 v[86:89], v[82:85], v[114:117], v[14:17] cbsz:4 blgp:4
	v_mfma_f32_16x16x128_f8f6f4 v[86:89], v[102:105], v[130:133], v[86:89] cbsz:4 blgp:4
	v_mfma_f32_16x16x128_f8f6f4 v[90:93], v[94:97], v[114:117], v[10:13] cbsz:4 blgp:4
	v_mfma_f32_16x16x128_f8f6f4 v[90:93], v[110:113], v[130:133], v[90:93] cbsz:4 blgp:4
	v_mfma_f32_16x16x128_f8f6f4 v[98:101], v[82:85], v[122:125], v[14:17] cbsz:4 blgp:4
	v_mfma_f32_16x16x128_f8f6f4 v[98:101], v[102:105], v[134:137], v[98:101] cbsz:4 blgp:4
	v_mfma_f32_16x16x128_f8f6f4 v[106:109], v[94:97], v[122:125], v[10:13] cbsz:4 blgp:4
	v_mfma_f32_16x16x128_f8f6f4 v[106:109], v[110:113], v[134:137], v[106:109] cbsz:4 blgp:4
	v_mfma_f32_16x16x128_f8f6f4 v[118:121], v[82:85], v[176:179], v[14:17] cbsz:4 blgp:4
	v_mfma_f32_16x16x128_f8f6f4 v[118:121], v[102:105], v[184:187], v[118:121] cbsz:4 blgp:4
	v_mfma_f32_16x16x128_f8f6f4 v[126:129], v[94:97], v[176:179], v[10:13] cbsz:4 blgp:4
	v_mfma_f32_16x16x128_f8f6f4 v[126:129], v[110:113], v[184:187], v[126:129] cbsz:4 blgp:4
	v_mfma_f32_16x16x128_f8f6f4 v[138:141], v[82:85], v[180:183], v[14:17] cbsz:4 blgp:4
	v_mfma_f32_16x16x128_f8f6f4 v[138:141], v[102:105], v[188:191], v[138:141] cbsz:4 blgp:4
	v_mfma_f32_16x16x128_f8f6f4 v[82:85], v[94:97], v[180:183], v[10:13] cbsz:4 blgp:4
	v_mfma_f32_16x16x128_f8f6f4 v[82:85], v[110:113], v[188:191], v[82:85] cbsz:4 blgp:4
	v_mfma_f32_16x16x128_f8f6f4 v[94:97], v[142:145], v[114:117], v[6:9] cbsz:4 blgp:4
	v_mfma_f32_16x16x128_f8f6f4 v[94:97], v[168:171], v[130:133], v[94:97] cbsz:4 blgp:4
	v_mfma_f32_16x16x128_f8f6f4 v[102:105], v[156:159], v[114:117], v[2:5] cbsz:4 blgp:4
	v_mfma_f32_16x16x128_f8f6f4 v[102:105], v[172:175], v[130:133], v[102:105] cbsz:4 blgp:4
	v_mfma_f32_16x16x128_f8f6f4 v[110:113], v[142:145], v[122:125], v[6:9] cbsz:4 blgp:4
	v_mfma_f32_16x16x128_f8f6f4 v[110:113], v[168:171], v[134:137], v[110:113] cbsz:4 blgp:4
	v_mfma_f32_16x16x128_f8f6f4 v[114:117], v[156:159], v[122:125], v[2:5] cbsz:4 blgp:4
	v_mfma_f32_16x16x128_f8f6f4 v[114:117], v[172:175], v[134:137], v[114:117] cbsz:4 blgp:4
	v_mfma_f32_16x16x128_f8f6f4 v[122:125], v[142:145], v[176:179], v[6:9] cbsz:4 blgp:4
	v_mfma_f32_16x16x128_f8f6f4 v[122:125], v[168:171], v[184:187], v[122:125] cbsz:4 blgp:4
	v_mfma_f32_16x16x128_f8f6f4 v[130:133], v[156:159], v[176:179], v[2:5] cbsz:4 blgp:4
	v_mfma_f32_16x16x128_f8f6f4 v[130:133], v[172:175], v[184:187], v[130:133] cbsz:4 blgp:4
	v_mfma_f32_16x16x128_f8f6f4 v[134:137], v[142:145], v[180:183], v[6:9] cbsz:4 blgp:4
	v_mfma_f32_16x16x128_f8f6f4 v[134:137], v[168:171], v[188:191], v[134:137] cbsz:4 blgp:4
	v_mfma_f32_16x16x128_f8f6f4 v[142:145], v[156:159], v[180:183], v[2:5] cbsz:4 blgp:4
	v_mfma_f32_16x16x128_f8f6f4 v[142:145], v[172:175], v[188:191], v[142:145] cbsz:4 blgp:4
	s_barrier
	s_add_i32 s54, s54, 1
	s_mul_i32 s0, s54, s73
	s_mul_hi_u32 s1, s54, s33
	s_add_i32 s1, s1, s0
	s_mul_i32 s0, s54, s33
	s_add_u32 s4, s0, s2
	s_addc_u32 s5, s1, s74
	v_mov_b64_e32 v[230:231], s[20:21]
	v_cmp_ge_i64_e32 vcc, s[4:5], v[230:231]
	s_and_b64 s[0:1], exec, vcc
	s_mov_b64 vcc, s[0:1]
	s_cbranch_vccnz .LBB5_7
	s_and_b32 s13, s4, 7
	s_lshl_b32 s13, s13, s37
	s_ashr_i32 s28, s4, 3
	s_add_i32 s13, s13, s28
	s_ashr_i32 s28, s13, s52
	s_and_b32 s13, s13, s63
	s_lshl_b32 s28, s28, 3
	s_and_b32 s29, s13, 7
	s_or_b32 s75, s28, s29
	s_ashr_i32 s28, s75, s53
	s_lshr_b32 s13, s13, 3
	s_mul_i32 s28, s28, s6
	s_and_b32 s76, s75, s7
	s_add_i32 s28, s28, s13
.LBB5_7:
	v_mov_b64_e32 v[230:231], s[20:21]
	v_cmp_lt_i64_e32 vcc, s[4:5], v[230:231]
	s_mov_b64 s[38:39], s[42:43]
	s_nop 0
	v_cndmask_b32_e64 v230, 0, 1, vcc
	v_cmp_ne_u32_e64 s[4:5], 1, v230
	s_andn2_b64 vcc, exec, vcc
	s_cbranch_vccz .LBB5_10
	s_and_b64 vcc, exec, s[4:5]
	s_mov_b64 s[4:5], s[40:41]
	s_cbranch_vccz .LBB5_11

.Lsd_5:
	ds_read_b128 v[156:159], v163 offset:32768
	ds_read_b128 v[168:171], v163 offset:34816
	ds_read_b128 v[172:175], v164 offset:32768
	ds_read_b128 v[176:179], v164 offset:34816
	ds_read_b128 v[180:183], v165 offset:32768
	ds_read_b128 v[184:187], v165 offset:34816
	ds_read_b128 v[188:191], v166 offset:32768
	ds_read_b128 v[192:195], v166 offset:34816
	ds_read_b128 v[196:199], v165 offset:36864
	ds_read_b128 v[200:203], v165 offset:38912
	ds_read_b128 v[204:207], v166 offset:36864
	ds_read_b128 v[208:211], v166 offset:38912
	s_add_u32 s48, s48, s22
	s_addc_u32 s49, s49, s23
	s_mov_b32 m0, s61
	s_nop 0
	global_load_lds_dwordx4 v146, s[48:49]
	s_mov_b32 m0, s62
	s_nop 0
	global_load_lds_dwordx4 v150, s[48:49]
	s_waitcnt lgkmcnt(8)
	ds_read_b128 v[212:215], v163 offset:49152
	ds_read_b128 v[216:219], v163 offset:51200
	ds_read_b128 v[220:223], v164 offset:49152
	ds_read_b128 v[224:227], v164 offset:51200
	s_waitcnt vmcnt(8)
	s_waitcnt lgkmcnt(0)
	s_barrier
	s_waitcnt lgkmcnt(0)
	v_mfma_f32_16x16x128_f8f6f4 v[18:21], v[156:159], v[180:183], v[18:21] cbsz:4 blgp:4
	v_mfma_f32_16x16x128_f8f6f4 v[18:21], v[172:175], v[188:191], v[18:21] cbsz:4 blgp:4
	v_mfma_f32_16x16x128_f8f6f4 v[22:25], v[168:171], v[180:183], v[22:25] cbsz:4 blgp:4
	v_mfma_f32_16x16x128_f8f6f4 v[22:25], v[176:179], v[188:191], v[22:25] cbsz:4 blgp:4
	v_mfma_f32_16x16x128_f8f6f4 v[26:29], v[156:159], v[184:187], v[26:29] cbsz:4 blgp:4
	v_mfma_f32_16x16x128_f8f6f4 v[26:29], v[172:175], v[192:195], v[26:29] cbsz:4 blgp:4
	v_mfma_f32_16x16x128_f8f6f4 v[30:33], v[168:171], v[184:187], v[30:33] cbsz:4 blgp:4
	v_mfma_f32_16x16x128_f8f6f4 v[30:33], v[176:179], v[192:195], v[30:33] cbsz:4 blgp:4
	v_mfma_f32_16x16x128_f8f6f4 v[34:37], v[156:159], v[196:199], v[34:37] cbsz:4 blgp:4
	v_mfma_f32_16x16x128_f8f6f4 v[34:37], v[172:175], v[204:207], v[34:37] cbsz:4 blgp:4
	v_mfma_f32_16x16x128_f8f6f4 v[38:41], v[168:171], v[196:199], v[38:41] cbsz:4 blgp:4
	v_mfma_f32_16x16x128_f8f6f4 v[38:41], v[176:179], v[204:207], v[38:41] cbsz:4 blgp:4
	v_mfma_f32_16x16x128_f8f6f4 v[42:45], v[156:159], v[200:203], v[42:45] cbsz:4 blgp:4
	v_mfma_f32_16x16x128_f8f6f4 v[42:45], v[172:175], v[208:211], v[42:45] cbsz:4 blgp:4
	v_mfma_f32_16x16x128_f8f6f4 v[46:49], v[168:171], v[200:203], v[46:49] cbsz:4 blgp:4
	v_mfma_f32_16x16x128_f8f6f4 v[46:49], v[176:179], v[208:211], v[46:49] cbsz:4 blgp:4
	v_mfma_f32_16x16x128_f8f6f4 v[50:53], v[212:215], v[180:183], v[50:53] cbsz:4 blgp:4
	v_mfma_f32_16x16x128_f8f6f4 v[50:53], v[220:223], v[188:191], v[50:53] cbsz:4 blgp:4
	v_mfma_f32_16x16x128_f8f6f4 v[54:57], v[216:219], v[180:183], v[54:57] cbsz:4 blgp:4
	v_mfma_f32_16x16x128_f8f6f4 v[54:57], v[224:227], v[188:191], v[54:57] cbsz:4 blgp:4
	v_mfma_f32_16x16x128_f8f6f4 v[58:61], v[212:215], v[184:187], v[58:61] cbsz:4 blgp:4
	v_mfma_f32_16x16x128_f8f6f4 v[58:61], v[220:223], v[192:195], v[58:61] cbsz:4 blgp:4
	v_mfma_f32_16x16x128_f8f6f4 v[62:65], v[216:219], v[184:187], v[62:65] cbsz:4 blgp:4
	v_mfma_f32_16x16x128_f8f6f4 v[62:65], v[224:227], v[192:195], v[62:65] cbsz:4 blgp:4
	v_mfma_f32_16x16x128_f8f6f4 v[66:69], v[212:215], v[196:199], v[66:69] cbsz:4 blgp:4
	v_mfma_f32_16x16x128_f8f6f4 v[66:69], v[220:223], v[204:207], v[66:69] cbsz:4 blgp:4
	v_mfma_f32_16x16x128_f8f6f4 v[70:73], v[216:219], v[196:199], v[70:73] cbsz:4 blgp:4
	v_mfma_f32_16x16x128_f8f6f4 v[70:73], v[224:227], v[204:207], v[70:73] cbsz:4 blgp:4
	v_mfma_f32_16x16x128_f8f6f4 v[74:77], v[212:215], v[200:203], v[74:77] cbsz:4 blgp:4
	v_mfma_f32_16x16x128_f8f6f4 v[74:77], v[220:223], v[208:211], v[74:77] cbsz:4 blgp:4
	v_mfma_f32_16x16x128_f8f6f4 v[78:81], v[216:219], v[200:203], v[78:81] cbsz:4 blgp:4
	v_mfma_f32_16x16x128_f8f6f4 v[78:81], v[224:227], v[208:211], v[78:81] cbsz:4 blgp:4
	s_barrier
	s_mov_b32 m0, s65
	s_nop 0
	global_load_lds_dwordx4 v148, s[44:45]
	s_mov_b32 m0, s66
	s_nop 0
	global_load_lds_dwordx4 v152, s[44:45]
	ds_read_b128 v[180:183], v165 offset:49152
	ds_read_b128 v[184:187], v165 offset:51200
	ds_read_b128 v[188:191], v166 offset:49152
	ds_read_b128 v[192:195], v166 offset:51200
	ds_read_b128 v[196:199], v165 offset:53248
	ds_read_b128 v[200:203], v165 offset:55296
	ds_read_b128 v[204:207], v166 offset:53248
	ds_read_b128 v[208:211], v166 offset:55296
	s_mov_b32 m0, s67
	s_nop 0
	global_load_lds_dwordx4 v146, s[46:47]
	s_mov_b32 m0, s68
	s_nop 0
	global_load_lds_dwordx4 v150, s[46:47]
	s_add_u32 s44, s44, s24
	s_addc_u32 s45, s45, s25
	s_mov_b32 m0, s69
	s_nop 0
	global_load_lds_dwordx4 v148, s[44:45]
	s_mov_b32 m0, s70
	s_nop 0
	global_load_lds_dwordx4 v152, s[44:45]
	s_waitcnt vmcnt(8)
	s_waitcnt lgkmcnt(0)
	s_barrier
	v_mfma_f32_16x16x128_f8f6f4 v[86:89], v[156:159], v[180:183], v[86:89] cbsz:4 blgp:4
	v_mfma_f32_16x16x128_f8f6f4 v[86:89], v[172:175], v[188:191], v[86:89] cbsz:4 blgp:4
	v_mfma_f32_16x16x128_f8f6f4 v[90:93], v[168:171], v[180:183], v[90:93] cbsz:4 blgp:4
	v_mfma_f32_16x16x128_f8f6f4 v[90:93], v[176:179], v[188:191], v[90:93] cbsz:4 blgp:4
	v_mfma_f32_16x16x128_f8f6f4 v[98:101], v[156:159], v[184:187], v[98:101] cbsz:4 blgp:4
	v_mfma_f32_16x16x128_f8f6f4 v[98:101], v[172:175], v[192:195], v[98:101] cbsz:4 blgp:4
	v_mfma_f32_16x16x128_f8f6f4 v[106:109], v[168:171], v[184:187], v[106:109] cbsz:4 blgp:4
	v_mfma_f32_16x16x128_f8f6f4 v[106:109], v[176:179], v[192:195], v[106:109] cbsz:4 blgp:4
	v_mfma_f32_16x16x128_f8f6f4 v[118:121], v[156:159], v[196:199], v[118:121] cbsz:4 blgp:4
	v_mfma_f32_16x16x128_f8f6f4 v[118:121], v[172:175], v[204:207], v[118:121] cbsz:4 blgp:4
	v_mfma_f32_16x16x128_f8f6f4 v[126:129], v[168:171], v[196:199], v[126:129] cbsz:4 blgp:4
	v_mfma_f32_16x16x128_f8f6f4 v[126:129], v[176:179], v[204:207], v[126:129] cbsz:4 blgp:4
	v_mfma_f32_16x16x128_f8f6f4 v[138:141], v[156:159], v[200:203], v[138:141] cbsz:4 blgp:4
	v_mfma_f32_16x16x128_f8f6f4 v[138:141], v[172:175], v[208:211], v[138:141] cbsz:4 blgp:4
	v_mfma_f32_16x16x128_f8f6f4 v[82:85], v[168:171], v[200:203], v[82:85] cbsz:4 blgp:4
	v_mfma_f32_16x16x128_f8f6f4 v[82:85], v[176:179], v[208:211], v[82:85] cbsz:4 blgp:4
	v_mfma_f32_16x16x128_f8f6f4 v[94:97], v[212:215], v[180:183], v[94:97] cbsz:4 blgp:4
	v_mfma_f32_16x16x128_f8f6f4 v[94:97], v[220:223], v[188:191], v[94:97] cbsz:4 blgp:4
	v_mfma_f32_16x16x128_f8f6f4 v[102:105], v[216:219], v[180:183], v[102:105] cbsz:4 blgp:4
	v_mfma_f32_16x16x128_f8f6f4 v[102:105], v[224:227], v[188:191], v[102:105] cbsz:4 blgp:4
	v_mfma_f32_16x16x128_f8f6f4 v[110:113], v[212:215], v[184:187], v[110:113] cbsz:4 blgp:4
	v_mfma_f32_16x16x128_f8f6f4 v[110:113], v[220:223], v[192:195], v[110:113] cbsz:4 blgp:4
	v_mfma_f32_16x16x128_f8f6f4 v[114:117], v[216:219], v[184:187], v[114:117] cbsz:4 blgp:4
	v_mfma_f32_16x16x128_f8f6f4 v[114:117], v[224:227], v[192:195], v[114:117] cbsz:4 blgp:4
	v_mfma_f32_16x16x128_f8f6f4 v[122:125], v[212:215], v[196:199], v[122:125] cbsz:4 blgp:4
	v_mfma_f32_16x16x128_f8f6f4 v[122:125], v[220:223], v[204:207], v[122:125] cbsz:4 blgp:4
	v_mfma_f32_16x16x128_f8f6f4 v[130:133], v[216:219], v[196:199], v[130:133] cbsz:4 blgp:4
	v_mfma_f32_16x16x128_f8f6f4 v[130:133], v[224:227], v[204:207], v[130:133] cbsz:4 blgp:4
	v_mfma_f32_16x16x128_f8f6f4 v[134:137], v[212:215], v[200:203], v[134:137] cbsz:4 blgp:4
	v_mfma_f32_16x16x128_f8f6f4 v[134:137], v[220:223], v[208:211], v[134:137] cbsz:4 blgp:4
	v_mfma_f32_16x16x128_f8f6f4 v[142:145], v[216:219], v[200:203], v[142:145] cbsz:4 blgp:4
	v_mfma_f32_16x16x128_f8f6f4 v[142:145], v[224:227], v[208:211], v[142:145] cbsz:4 blgp:4
	s_andn2_b64 vcc, exec, s[34:35]
	s_barrier
	s_cbranch_vccnz .LBB5_4
	s_ashr_i32 s29, s28, 31
	s_lshl_b64 s[44:45], s[28:29], 10
	s_add_u32 s44, s10, s44
	s_addc_u32 s45, s11, s45
	s_add_u32 s29, s42, 0x200
	s_addc_u32 s79, s43, 0
	s_add_u32 s80, s40, 0x200
	s_addc_u32 s81, s41, 0
	s_add_u32 s40, s82, 0x180
	s_addc_u32 s41, s83, 0
	s_mov_b32 s82, 4
	s_cmp_eq_u32 s64, s82
	s_cselect_b64 s[42:43], -1, 0
	s_cmp_lg_u32 s64, s82
	s_cbranch_scc1 .LBB5_15

amdhsa.kernels:
  - .agpr_count:     0
    .args:
      - .offset:         0
        .size:           80
        .value_kind:     by_value
    .group_segment_fixed_size: 8192
    .kernarg_segment_align: 8
    .kernarg_segment_size: 80
    .language:       OpenCL C
    .language_version:
      - 2
      - 0
    .max_flat_workgroup_size: 256
    .name:           _Z6k_prep8PrepArgs
    .private_segment_fixed_size: 0
    .sgpr_count:     35
    .sgpr_spill_count: 0
    .symbol:         _Z6k_prep8PrepArgs.kd
    .uniform_work_group_size: 1
    .uses_dynamic_stack: false
    .vgpr_count:     45
    .vgpr_spill_count: 0
    .wavefront_size: 64
  - .agpr_count:     4
    .args:
      - .actual_access:  read_only
        .address_space:  global
        .offset:         0
        .size:           8
        .value_kind:     global_buffer
      - .actual_access:  read_only
        .address_space:  global
        .offset:         8
        .size:           8
        .value_kind:     global_buffer
      - .actual_access:  read_only
        .address_space:  global
        .offset:         16
        .size:           8
        .value_kind:     global_buffer
      - .actual_access:  write_only
        .address_space:  global
        .offset:         24
        .size:           8
        .value_kind:     global_buffer
      - .actual_access:  write_only
        .address_space:  global
        .offset:         32
        .size:           8
        .value_kind:     global_buffer
    .group_segment_fixed_size: 36096
    .kernarg_segment_align: 8
    .kernarg_segment_size: 40
    .language:       OpenCL C
    .language_version:
      - 2
      - 0
    .max_flat_workgroup_size: 256
    .name:           _Z7k_gatesPKfPKtS0_PhPf
    .private_segment_fixed_size: 0
    .sgpr_count:     18
    .sgpr_spill_count: 0
    .symbol:         _Z7k_gatesPKfPKtS0_PhPf.kd
    .uniform_work_group_size: 1
    .uses_dynamic_stack: false
    .vgpr_count:     88
    .vgpr_spill_count: 0
    .wavefront_size: 64
  - .agpr_count:     0
    .args:
      - .actual_access:  read_only
        .address_space:  global
        .offset:         0
        .size:           8
        .value_kind:     global_buffer
      - .actual_access:  read_only
        .address_space:  global
        .offset:         8
        .size:           8
        .value_kind:     global_buffer
      - .actual_access:  write_only
        .address_space:  global
        .offset:         16
        .size:           8
        .value_kind:     global_buffer
      - .offset:         24
        .size:           4
        .value_kind:     by_value
    .group_segment_fixed_size: 0
    .kernarg_segment_align: 8
    .kernarg_segment_size: 28
    .language:       OpenCL C
    .language_version:
      - 2
      - 0
    .max_flat_workgroup_size: 256
    .name:           _Z5k_mixPKhPKfPhi
    .private_segment_fixed_size: 0
    .sgpr_count:     14
    .sgpr_spill_count: 0
    .symbol:         _Z5k_mixPKhPKfPhi.kd
    .uniform_work_group_size: 1
    .uses_dynamic_stack: false
    .vgpr_count:     126
    .vgpr_spill_count: 0
    .wavefront_size: 64
  - .agpr_count:     0
    .args:
      - .actual_access:  read_only
        .address_space:  global
        .offset:         0
        .size:           8
        .value_kind:     global_buffer
      - .actual_access:  read_only
        .address_space:  global
        .offset:         8
        .size:           8
        .value_kind:     global_buffer
      - .actual_access:  write_only
        .address_space:  global
        .offset:         16
        .size:           8
        .value_kind:     global_buffer
    .group_segment_fixed_size: 0
    .kernarg_segment_align: 8
    .kernarg_segment_size: 24
    .language:       OpenCL C
    .language_version:
      - 2
      - 0
    .max_flat_workgroup_size: 256
    .name:           _Z7k_finalPKfS0_Pf
    .private_segment_fixed_size: 0
    .sgpr_count:     16
    .sgpr_spill_count: 0
    .symbol:         _Z7k_finalPKfS0_Pf.kd
    .uniform_work_group_size: 1
    .uses_dynamic_stack: false
    .vgpr_count:     16
    .vgpr_spill_count: 0
    .wavefront_size: 64
  - .agpr_count:     0
    .args:
      - .offset:         0
        .size:           24
        .value_kind:     by_value
      - .offset:         24
        .size:           32
        .value_kind:     by_value
      - .offset:         56
        .size:           4
        .value_kind:     by_value
      - .offset:         60
        .size:           4
        .value_kind:     by_value
      - .offset:         64
        .size:           4
        .value_kind:     by_value
      - .offset:         68
        .size:           4
        .value_kind:     by_value
      - .offset:         72
        .size:           4
        .value_kind:     hidden_block_count_x
      - .offset:         76
        .size:           4
        .value_kind:     hidden_block_count_y
      - .offset:         80
        .size:           4
        .value_kind:     hidden_block_count_z
      - .offset:         84
        .size:           2
        .value_kind:     hidden_group_size_x
      - .offset:         86
        .size:           2
        .value_kind:     hidden_group_size_y
      - .offset:         88
        .size:           2
        .value_kind:     hidden_group_size_z
      - .offset:         90
        .size:           2
        .value_kind:     hidden_remainder_x
      - .offset:         92
        .size:           2
        .value_kind:     hidden_remainder_y
      - .offset:         94
        .size:           2
        .value_kind:     hidden_remainder_z
      - .offset:         112
        .size:           8
        .value_kind:     hidden_global_offset_x
      - .offset:         120
        .size:           8
        .value_kind:     hidden_global_offset_y
      - .offset:         128
        .size:           8
        .value_kind:     hidden_global_offset_z
      - .offset:         136
        .size:           2
        .value_kind:     hidden_grid_dims
      - .offset:         192
        .size:           4
        .value_kind:     hidden_dynamic_lds_size
    .group_segment_fixed_size: 0
    .kernarg_segment_align: 8
    .kernarg_segment_size: 328
    .language:       OpenCL C
    .language_version:
      - 2
      - 0
    .max_flat_workgroup_size: 512
    .name:           _Z6k_gemmI4Epi8ILi0ELb1ELb1EEEv4GemmT_iiii
    .private_segment_fixed_size: 0
    .sgpr_count:     89
    .sgpr_spill_count: 0
    .symbol:         _Z6k_gemmI4Epi8ILi0ELb1ELb1EEEv4GemmT_iiii.kd
    .uniform_work_group_size: 1
    .uses_dynamic_stack: false
    .vgpr_count:     232
    .vgpr_spill_count: 0
    .wavefront_size: 64
  - .agpr_count:     0
    .args:
      - .offset:         0
        .size:           24
        .value_kind:     by_value
      - .offset:         24
        .size:           32
        .value_kind:     by_value
      - .offset:         56
        .size:           4
        .value_kind:     by_value
      - .offset:         60
        .size:           4
        .value_kind:     by_value
      - .offset:         64
        .size:           4
        .value_kind:     by_value
      - .offset:         68
        .size:           4
        .value_kind:     by_value
      - .offset:         72
        .size:           4
        .value_kind:     hidden_block_count_x
      - .offset:         76
        .size:           4
        .value_kind:     hidden_block_count_y
      - .offset:         80
        .size:           4
        .value_kind:     hidden_block_count_z
      - .offset:         84
        .size:           2
        .value_kind:     hidden_group_size_x
      - .offset:         86
        .size:           2
        .value_kind:     hidden_group_size_y
      - .offset:         88
        .size:           2
        .value_kind:     hidden_group_size_z
      - .offset:         90
        .size:           2
        .value_kind:     hidden_remainder_x
      - .offset:         92
        .size:           2
        .value_kind:     hidden_remainder_y
      - .offset:         94
        .size:           2
        .value_kind:     hidden_remainder_z
      - .offset:         112
        .size:           8
        .value_kind:     hidden_global_offset_x
      - .offset:         120
        .size:           8
        .value_kind:     hidden_global_offset_y
      - .offset:         128
        .size:           8
        .value_kind:     hidden_global_offset_z
      - .offset:         136
        .size:           2
        .value_kind:     hidden_grid_dims
      - .offset:         192
        .size:           4
        .value_kind:     hidden_dynamic_lds_size
    .group_segment_fixed_size: 0
    .kernarg_segment_align: 8
    .kernarg_segment_size: 328
    .language:       OpenCL C
    .language_version:
      - 2
      - 0
    .max_flat_workgroup_size: 512
    .name:           _Z6k_gemmI4Epi8ILi1ELb1ELb1EEEv4GemmT_iiii
    .private_segment_fixed_size: 0
    .sgpr_count:     90
    .sgpr_spill_count: 0
    .symbol:         _Z6k_gemmI4Epi8ILi1ELb1ELb1EEEv4GemmT_iiii.kd
    .uniform_work_group_size: 1
    .uses_dynamic_stack: false
    .vgpr_count:     232
    .vgpr_spill_count: 0
    .wavefront_size: 64
  - .agpr_count:     0
    .args:
      - .offset:         0
        .size:           24
        .value_kind:     by_value
      - .offset:         24
        .size:           32
        .value_kind:     by_value
      - .offset:         56
        .size:           4
        .value_kind:     by_value
      - .offset:         60
        .size:           4
        .value_kind:     by_value
      - .offset:         64
        .size:           4
        .value_kind:     by_value
      - .offset:         68
        .size:           4
        .value_kind:     by_value
      - .offset:         72
        .size:           4
        .value_kind:     hidden_block_count_x
      - .offset:         76
        .size:           4
        .value_kind:     hidden_block_count_y
      - .offset:         80
        .size:           4
        .value_kind:     hidden_block_count_z
      - .offset:         84
        .size:           2
        .value_kind:     hidden_group_size_x
      - .offset:         86
        .size:           2
        .value_kind:     hidden_group_size_y
      - .offset:         88
        .size:           2
        .value_kind:     hidden_group_size_z
      - .offset:         90
        .size:           2
        .value_kind:     hidden_remainder_x
      - .offset:         92
        .size:           2
        .value_kind:     hidden_remainder_y
      - .offset:         94
        .size:           2
        .value_kind:     hidden_remainder_z
      - .offset:         112
        .size:           8
        .value_kind:     hidden_global_offset_x
      - .offset:         120
        .size:           8
        .value_kind:     hidden_global_offset_y
      - .offset:         128
        .size:           8
        .value_kind:     hidden_global_offset_z
      - .offset:         136
        .size:           2
        .value_kind:     hidden_grid_dims
      - .offset:         192
        .size:           4
        .value_kind:     hidden_dynamic_lds_size
    .group_segment_fixed_size: 0
    .kernarg_segment_align: 8
    .kernarg_segment_size: 328
    .language:       OpenCL C
    .language_version:
      - 2
      - 0
    .max_flat_workgroup_size: 512
    .name:           _Z6k_gemmI8EpiTowerEv4GemmT_iiii
    .private_segment_fixed_size: 0
    .sgpr_count:     92
    .sgpr_spill_count: 0
    .symbol:         _Z6k_gemmI8EpiTowerEv4GemmT_iiii.kd
    .uniform_work_group_size: 1
    .uses_dynamic_stack: false
    .vgpr_count:     230
    .vgpr_spill_count: 0
    .wavefront_size: 64
